# removed dead VALU in phase 2; phase 0 LDS addresses precomputed before the load wait (2 base + xor32 + imm offsets), hand-written convert blocks
# speedup vs baseline: 1.0000x; 1.0000x over previous
_Z7na_mainPKDF16_PKhS0_PKfS4_S4_S4_Pf:
	s_lshl_b32 s3, s2, 5
	s_and_b32 s3, s3, 0xe0
	s_ashr_i32 s2, s2, 3
	s_add_i32 s3, s3, s2
	s_ashr_i32 s2, s3, 6
	s_lshl_b32 s3, s3, 5
	s_and_b32 s14, s3, 0x7e0
	v_mov_b32_e32 v1, 0x7c0
	s_load_dwordx8 s[4:11], s[0:1], 0x0
	s_load_dwordx2 s[18:19], s[0:1], 0x20
	v_med3_u32 v1, s14, 32, v1
	v_subrev_u32_e32 v97, 32, v1
	s_ashr_i32 s3, s2, 31
	v_lshlrev_b32_e32 v58, 1, v97
	s_lshl_b64 s[12:13], s[2:3], 12
	v_mov_b32_e32 v59, 0
	v_sub_u32_e32 v60, s14, v97
	v_lshl_add_u64 v[10:11], s[12:13], 0, v[58:59]
	v_lshlrev_b64 v[2:3], 9, v[10:11]
	v_lshl_or_b32 v22, v60, 6, v0
	s_waitcnt lgkmcnt(0)
	v_and_b32_e32 v208, 31, v0
	v_lshlrev_b32_e32 v208, 5, v208
	global_load_dwordx4 v[192:195], v208, s[18:19]
	global_load_dwordx4 v[196:199], v208, s[18:19] offset:16
	v_lshl_add_u64 v[20:21], s[4:5], 0, v[2:3]
	v_ashrrev_i32_e32 v23, 31, v22
	v_lshl_add_u64 v[2:3], v[22:23], 4, v[20:21]
	global_load_dwordx4 v[12:15], v[2:3], off
	v_or_b32_e32 v28, 0x200, v22
	v_ashrrev_i32_e32 v29, 31, v28
	v_lshl_add_u64 v[2:3], v[28:29], 4, v[20:21]
	global_load_dwordx4 v[16:19], v[2:3], off
	v_or_b32_e32 v184, 0x400, v22
	v_ashrrev_i32_e32 v185, 31, v184
	v_lshl_add_u64 v[184:185], v[184:185], 4, v[20:21]
	v_or_b32_e32 v188, 0x600, v22
	v_ashrrev_i32_e32 v189, 31, v188
	v_lshl_add_u64 v[188:189], v[188:189], 4, v[20:21]
	global_load_dwordx4 v[184:187], v[184:185], off
	global_load_dwordx4 v[188:191], v[188:189], off
	v_lshrrev_b32_e32 v99, 6, v0
	v_and_b32_e32 v98, 63, v0
	v_lshlrev_b32_e32 v118, 13, v99
	v_lshl_or_b32 v58, v98, 5, v118
	s_movk_i32 s15, 0x1000
	v_lshl_add_u64 v[24:25], s[6:7], 0, v[58:59]
	v_or_b32_e32 v32, 0x400, v22
	v_or_b32_e32 v62, 0x600, v22
	v_add_co_u32_e32 v64, vcc, s15, v24
	s_mov_b64 s[12:13], 0x1000
	s_mov_b64 s[16:17], 0x1800
	v_lshlrev_b32_e32 v72, 1, v60
	v_lshrrev_b32_e32 v23, 5, v22
	v_and_b32_e32 v34, 32, v22
	v_ashrrev_i32_e32 v33, 31, v32
	v_ashrrev_i32_e32 v63, 31, v62
	v_addc_co_u32_e32 v65, vcc, 0, v25, vcc
	global_load_dwordx4 v[6:9], v58, s[6:7] offset:16
	global_load_dwordx4 v[2:5], v58, s[6:7]
	global_load_dwordx4 v[54:57], v58, s[6:7] offset:2064
	global_load_dwordx4 v[50:53], v58, s[6:7] offset:2048
	v_lshrrev_b32_e32 v58, 6, v22
	v_bfe_u32 v73, v22, 8, 2
	v_lshl_add_u64 v[26:27], v[24:25], 0, s[12:13]
	v_lshl_add_u64 v[24:25], v[24:25], 0, s[16:17]
	v_cmp_ne_u32_e32 vcc, 0, v34
	v_sub_u32_e32 v75, v23, v72
	global_load_dwordx4 v[42:45], v[64:65], off
	global_load_dwordx4 v[46:49], v[26:27], off offset:16
	global_load_dwordx4 v[34:37], v[64:65], off offset:2048
	global_load_dwordx4 v[38:41], v[24:25], off offset:16
	v_mov_b32_e32 v61, 0x60
	v_cndmask_b32_e32 v74, 0, v61, vcc
	v_add_u32_e32 v33, v74, v58
	v_lshlrev_b32_e32 v64, 2, v33
	v_bfe_u32 v96, v0, 4, 1
	v_and_b32_e32 v100, 15, v0
	v_mov_b32_e32 v30, v59
	v_mov_b32_e32 v31, v59
	v_and_b32_e32 v64, 12, v64
	v_mul_u32_u24_e32 v29, 0xc000, v96
	v_bitop3_b32 v64, v64, v100, v73 bitop3:0x36
	v_lshl_or_b32 v64, v64, 4, v29
	v_lshlrev_b32_e32 v63, 1, v75
	v_lshl_add_u32 v33, v33, 8, v64
	v_bfe_u32 v71, v0, 1, 4
	v_and_b32_e32 v70, 32, v0
	v_lshlrev_b32_e32 v1, 3, v0
	v_lshrrev_b32_e32 v58, 1, v75
	v_and_b32_e32 v1, 8, v1
	v_add_lshl_u32 v58, v58, v70, 8
	v_lshlrev_b32_e32 v121, 3, v99
	v_bfe_u32 v101, v0, 4, 2
	v_lshlrev_b32_e32 v102, 2, v101
	v_and_b32_e32 v116, 31, v0
	v_bfe_u32 v119, v0, 5, 1
	v_lshlrev_b32_e32 v124, 1, v119
	v_lshlrev_b32_e32 v117, 8, v116
	v_lshrrev_b32_e32 v95, 4, v0
	s_movk_i32 s16, 0x60
	s_mov_b32 s17, 0xc000
	v_and_b32_e32 v211, 3, v99
	v_lshrrev_b32_e32 v212, 2, v99
	v_lshl_or_b32 v211, v211, 2, v212
	v_xor_b32_e32 v213, v100, v211
	v_mul_u32_u24_e32 v214, 0x60, v119
	v_add3_u32 v214, v214, v60, v99
	v_mul_u32_u24_e32 v215, 0xc000, v96
	v_lshl_add_u32 v214, v214, 8, v215
	v_lshl_or_b32 v220, v213, 4, v214
	v_xor_b32_e32 v221, 32, v220
	v_xor_b32_e32 v216, v71, v211
	v_lshl_add_u32 v217, v119, 5, v99
	v_lshlrev_b32_e32 v217, 8, v217
	v_lshl_or_b32 v216, v216, 4, v217
	v_or_b32_e32 v216, v216, v1
	v_add_u32_e32 v222, 0x23800, v216
	v_xor_b32_e32 v223, 32, v222
	s_waitcnt vmcnt(11)
	ds_write_b128 v220, v[12:15]
	v_fma_mix_f32 v200, v192, v12, 0 op_sel_hi:[0,1,0]
	v_fma_mix_f32 v201, v193, v12, 0 op_sel:[0,1,0] op_sel_hi:[0,1,0]
	v_cvt_f32_f16_e32 v211, v12
	v_cvt_f32_f16_sdwa v212, v12 dst_sel:DWORD dst_unused:UNUSED_PAD src0_sel:WORD_1
	v_fma_mix_f32 v200, v194, v13, v200 op_sel_hi:[0,1,0]
	v_fma_mix_f32 v201, v195, v13, v201 op_sel:[0,1,0] op_sel_hi:[0,1,0]
	v_cvt_f32_f16_e32 v213, v13
	v_cvt_f32_f16_sdwa v214, v13 dst_sel:DWORD dst_unused:UNUSED_PAD src0_sel:WORD_1
	v_fma_mix_f32 v200, v196, v14, v200 op_sel_hi:[0,1,0]
	v_fma_mix_f32 v201, v197, v14, v201 op_sel:[0,1,0] op_sel_hi:[0,1,0]
	v_cvt_f32_f16_e32 v215, v14
	v_cvt_f32_f16_sdwa v216, v14 dst_sel:DWORD dst_unused:UNUSED_PAD src0_sel:WORD_1
	v_fma_mix_f32 v200, v198, v15, v200 op_sel_hi:[0,1,0]
	v_fma_mix_f32 v201, v199, v15, v201 op_sel:[0,1,0] op_sel_hi:[0,1,0]
	v_cvt_f32_f16_e32 v217, v15
	v_cvt_f32_f16_sdwa v218, v15 dst_sel:DWORD dst_unused:UNUSED_PAD src0_sel:WORD_1
	v_cvt_pk_fp8_f32 v224, v211, v212
	v_cvt_pk_fp8_f32 v225, v215, v216
	v_cvt_pk_fp8_f32 v224, v213, v214 op_sel:[0,0,1]
	v_cvt_pk_fp8_f32 v225, v217, v218 op_sel:[0,0,1]
	s_nop 0
	ds_write_b64 v222, v[224:225]
	s_waitcnt vmcnt(10)
	ds_write_b128 v221, v[16:19] offset:2048
	v_fma_mix_f32 v202, v192, v16, 0 op_sel_hi:[0,1,0]
	v_fma_mix_f32 v203, v193, v16, 0 op_sel:[0,1,0] op_sel_hi:[0,1,0]
	v_cvt_f32_f16_e32 v211, v16
	v_cvt_f32_f16_sdwa v212, v16 dst_sel:DWORD dst_unused:UNUSED_PAD src0_sel:WORD_1
	v_fma_mix_f32 v202, v194, v17, v202 op_sel_hi:[0,1,0]
	v_fma_mix_f32 v203, v195, v17, v203 op_sel:[0,1,0] op_sel_hi:[0,1,0]
	v_cvt_f32_f16_e32 v213, v17
	v_cvt_f32_f16_sdwa v214, v17 dst_sel:DWORD dst_unused:UNUSED_PAD src0_sel:WORD_1
	v_fma_mix_f32 v202, v196, v18, v202 op_sel_hi:[0,1,0]
	v_fma_mix_f32 v203, v197, v18, v203 op_sel:[0,1,0] op_sel_hi:[0,1,0]
	v_cvt_f32_f16_e32 v215, v18
	v_cvt_f32_f16_sdwa v216, v18 dst_sel:DWORD dst_unused:UNUSED_PAD src0_sel:WORD_1
	v_fma_mix_f32 v202, v198, v19, v202 op_sel_hi:[0,1,0]
	v_fma_mix_f32 v203, v199, v19, v203 op_sel:[0,1,0] op_sel_hi:[0,1,0]
	v_cvt_f32_f16_e32 v217, v19
	v_cvt_f32_f16_sdwa v218, v19 dst_sel:DWORD dst_unused:UNUSED_PAD src0_sel:WORD_1
	v_cvt_pk_fp8_f32 v226, v211, v212
	v_cvt_pk_fp8_f32 v227, v215, v216
	v_cvt_pk_fp8_f32 v226, v213, v214 op_sel:[0,0,1]
	v_cvt_pk_fp8_f32 v227, v217, v218 op_sel:[0,0,1]
	s_nop 0
	ds_write_b64 v223, v[226:227] offset:2048
	s_waitcnt vmcnt(9)
	ds_write_b128 v220, v[184:187] offset:4096
	v_fma_mix_f32 v204, v192, v184, 0 op_sel_hi:[0,1,0]
	v_fma_mix_f32 v205, v193, v184, 0 op_sel:[0,1,0] op_sel_hi:[0,1,0]
	v_cvt_f32_f16_e32 v211, v184
	v_cvt_f32_f16_sdwa v212, v184 dst_sel:DWORD dst_unused:UNUSED_PAD src0_sel:WORD_1
	v_fma_mix_f32 v204, v194, v185, v204 op_sel_hi:[0,1,0]
	v_fma_mix_f32 v205, v195, v185, v205 op_sel:[0,1,0] op_sel_hi:[0,1,0]
	v_cvt_f32_f16_e32 v213, v185
	v_cvt_f32_f16_sdwa v214, v185 dst_sel:DWORD dst_unused:UNUSED_PAD src0_sel:WORD_1
	v_fma_mix_f32 v204, v196, v186, v204 op_sel_hi:[0,1,0]
	v_fma_mix_f32 v205, v197, v186, v205 op_sel:[0,1,0] op_sel_hi:[0,1,0]
	v_cvt_f32_f16_e32 v215, v186
	v_cvt_f32_f16_sdwa v216, v186 dst_sel:DWORD dst_unused:UNUSED_PAD src0_sel:WORD_1
	v_fma_mix_f32 v204, v198, v187, v204 op_sel_hi:[0,1,0]
	v_fma_mix_f32 v205, v199, v187, v205 op_sel:[0,1,0] op_sel_hi:[0,1,0]
	v_cvt_f32_f16_e32 v217, v187
	v_cvt_f32_f16_sdwa v218, v187 dst_sel:DWORD dst_unused:UNUSED_PAD src0_sel:WORD_1
	v_cvt_pk_fp8_f32 v228, v211, v212
	v_cvt_pk_fp8_f32 v229, v215, v216
	v_cvt_pk_fp8_f32 v228, v213, v214 op_sel:[0,0,1]
	v_cvt_pk_fp8_f32 v229, v217, v218 op_sel:[0,0,1]
	s_nop 0
	ds_write_b64 v222, v[228:229] offset:4096
	s_waitcnt vmcnt(8)
	ds_write_b128 v221, v[188:191] offset:6144
	v_fma_mix_f32 v206, v192, v188, 0 op_sel_hi:[0,1,0]
	v_fma_mix_f32 v207, v193, v188, 0 op_sel:[0,1,0] op_sel_hi:[0,1,0]
	v_cvt_f32_f16_e32 v211, v188
	v_cvt_f32_f16_sdwa v212, v188 dst_sel:DWORD dst_unused:UNUSED_PAD src0_sel:WORD_1
	v_fma_mix_f32 v206, v194, v189, v206 op_sel_hi:[0,1,0]
	v_fma_mix_f32 v207, v195, v189, v207 op_sel:[0,1,0] op_sel_hi:[0,1,0]
	v_cvt_f32_f16_e32 v213, v189
	v_cvt_f32_f16_sdwa v214, v189 dst_sel:DWORD dst_unused:UNUSED_PAD src0_sel:WORD_1
	v_fma_mix_f32 v206, v196, v190, v206 op_sel_hi:[0,1,0]
	v_fma_mix_f32 v207, v197, v190, v207 op_sel:[0,1,0] op_sel_hi:[0,1,0]
	v_cvt_f32_f16_e32 v215, v190
	v_cvt_f32_f16_sdwa v216, v190 dst_sel:DWORD dst_unused:UNUSED_PAD src0_sel:WORD_1
	v_fma_mix_f32 v206, v198, v191, v206 op_sel_hi:[0,1,0]
	v_fma_mix_f32 v207, v199, v191, v207 op_sel:[0,1,0] op_sel_hi:[0,1,0]
	v_cvt_f32_f16_e32 v217, v191
	v_cvt_f32_f16_sdwa v218, v191 dst_sel:DWORD dst_unused:UNUSED_PAD src0_sel:WORD_1
	v_cvt_pk_fp8_f32 v230, v211, v212
	v_cvt_pk_fp8_f32 v231, v215, v216
	v_cvt_pk_fp8_f32 v230, v213, v214 op_sel:[0,0,1]
	v_cvt_pk_fp8_f32 v231, v217, v218 op_sel:[0,0,1]
	s_nop 0
	ds_write_b64 v223, v[230:231] offset:6144
	v_add_f32_e32 v200, v200, v201
	v_add_f32_e32 v202, v202, v203
	v_add_f32_e32 v204, v204, v205
	v_add_f32_e32 v206, v206, v207
	v_lshlrev_b32_e32 v208, 7, v119
	v_lshl_add_u32 v208, v99, 2, v208
	v_add_u32_e32 v208, 0x27800, v208
	v_add_f32_dpp v200, v200, v200 quad_perm:[1,0,3,2] row_mask:0xf bank_mask:0xf
	v_add_f32_dpp v202, v202, v202 quad_perm:[1,0,3,2] row_mask:0xf bank_mask:0xf
	v_add_f32_dpp v204, v204, v204 quad_perm:[1,0,3,2] row_mask:0xf bank_mask:0xf
	v_add_f32_dpp v206, v206, v206 quad_perm:[1,0,3,2] row_mask:0xf bank_mask:0xf
	v_add_f32_dpp v200, v200, v200 quad_perm:[2,3,0,1] row_mask:0xf bank_mask:0xf
	v_add_f32_dpp v202, v202, v202 quad_perm:[2,3,0,1] row_mask:0xf bank_mask:0xf
	v_add_f32_dpp v204, v204, v204 quad_perm:[2,3,0,1] row_mask:0xf bank_mask:0xf
	v_add_f32_dpp v206, v206, v206 quad_perm:[2,3,0,1] row_mask:0xf bank_mask:0xf
	v_add_f32_dpp v200, v200, v200 row_half_mirror row_mask:0xf bank_mask:0xf
	v_add_f32_dpp v202, v202, v202 row_half_mirror row_mask:0xf bank_mask:0xf
	v_add_f32_dpp v204, v204, v204 row_half_mirror row_mask:0xf bank_mask:0xf
	v_add_f32_dpp v206, v206, v206 row_half_mirror row_mask:0xf bank_mask:0xf
	v_add_f32_dpp v200, v200, v200 row_mirror row_mask:0xf bank_mask:0xf
	v_add_f32_dpp v202, v202, v202 row_mirror row_mask:0xf bank_mask:0xf
	v_add_f32_dpp v204, v204, v204 row_mirror row_mask:0xf bank_mask:0xf
	v_add_f32_dpp v206, v206, v206 row_mirror row_mask:0xf bank_mask:0xf
	v_add_f32_dpp v200, v200, v200 row_bcast:15 row_mask:0xa bank_mask:0xf
	v_add_f32_dpp v202, v202, v202 row_bcast:15 row_mask:0xa bank_mask:0xf
	v_add_f32_dpp v204, v204, v204 row_bcast:15 row_mask:0xa bank_mask:0xf
	v_add_f32_dpp v206, v206, v206 row_bcast:15 row_mask:0xa bank_mask:0xf
	s_mov_b32 exec_lo, 0xffff0000
	s_mov_b32 exec_hi, 0xffff0000
	ds_write_b32 v208, v200
	ds_write_b32 v208, v202 offset:32
	ds_write_b32 v208, v204 offset:64
	ds_write_b32 v208, v206 offset:96
	s_mov_b64 exec, -1
	v_cmp_lt_i32_e32 vcc, v121, v60
	s_nop 0
	v_mov_b32_e32 v15, v59
	v_cndmask_b32_e64 v12, 32, 0, vcc
	v_add_u32_e32 v16, v12, v121
	v_or_b32_e32 v12, v16, v101
	v_lshlrev_b32_e32 v58, 1, v12
	v_lshrrev_b32_e32 v12, 5, v0
	v_and_b32_e32 v12, 2, v12
	v_bitop3_b32 v14, v102, v100, v12 bitop3:0x36
	v_lshl_add_u64 v[12:13], v[10:11], 0, v[58:59]
	v_lshlrev_b64 v[12:13], 9, v[12:13]
	v_lshlrev_b32_e32 v16, 8, v16
	v_lshl_add_u64 v[12:13], s[4:5], 0, v[12:13]
	v_lshlrev_b32_e32 v14, 4, v14
	v_readfirstlane_b32 s6, v16
	v_add_u32_e32 v17, 0xc000, v16
	v_lshl_add_u64 v[12:13], v[12:13], 0, v[14:15]
	s_mov_b32 m0, s6
	s_mov_b64 s[6:7], 0x100
	v_readfirstlane_b32 s12, v17
	global_load_lds_dwordx4 v[12:13], off
	v_lshl_add_u64 v[12:13], v[12:13], 0, s[6:7]
	s_mov_b32 m0, s12
	v_or_b32_e32 v58, 1, v58
	global_load_lds_dwordx4 v[12:13], off
	v_lshl_add_u64 v[12:13], v[10:11], 0, v[58:59]
	v_lshlrev_b64 v[12:13], 9, v[12:13]
	v_lshl_add_u64 v[12:13], s[4:5], 0, v[12:13]
	v_lshl_add_u64 v[12:13], v[12:13], 0, v[14:15]
	v_add_u32_e32 v14, 0x6000, v16
	v_bfe_u32 v61, v0, 2, 2
	v_readfirstlane_b32 s12, v14
	v_add_u32_e32 v14, 0x12000, v16
	s_mov_b32 m0, s12
	v_readfirstlane_b32 s12, v14
	global_load_lds_dwordx4 v[12:13], off
	v_lshl_add_u64 v[12:13], v[12:13], 0, s[6:7]
	s_mov_b32 m0, s12
	v_add_u32_e32 v18, 0x23800, v117
	global_load_lds_dwordx4 v[12:13], off
	v_or_b32_e32 v12, 4, v121
	v_cmp_lt_i32_e32 vcc, v12, v60
	s_nop 1
	v_cndmask_b32_e64 v13, 32, 0, vcc
	v_add_u32_e32 v16, v13, v12
	v_or_b32_e32 v13, v16, v101
	v_lshlrev_b32_e32 v58, 1, v13
	v_bfe_u32 v12, v12, 2, 2
	v_bitop3_b32 v14, v102, v100, v12 bitop3:0x36
	v_lshl_add_u64 v[12:13], v[10:11], 0, v[58:59]
	v_lshlrev_b64 v[12:13], 9, v[12:13]
	v_lshlrev_b32_e32 v16, 8, v16
	v_lshl_add_u64 v[12:13], s[4:5], 0, v[12:13]
	v_lshlrev_b32_e32 v14, 4, v14
	v_readfirstlane_b32 s12, v16
	v_add_u32_e32 v17, 0xc000, v16
	v_lshl_add_u64 v[12:13], v[12:13], 0, v[14:15]
	s_mov_b32 m0, s12
	v_readfirstlane_b32 s12, v17
	v_or_b32_e32 v58, 1, v58
	global_load_lds_dwordx4 v[12:13], off
	v_lshl_add_u64 v[12:13], v[12:13], 0, s[6:7]
	s_mov_b32 m0, s12
	v_lshl_add_u64 v[10:11], v[10:11], 0, v[58:59]
	global_load_lds_dwordx4 v[12:13], off
	v_lshlrev_b64 v[10:11], 9, v[10:11]
	v_add_u32_e32 v12, 0x6000, v16
	v_lshl_add_u64 v[10:11], s[4:5], 0, v[10:11]
	v_readfirstlane_b32 s4, v12
	v_add_u32_e32 v12, 0x12000, v16
	v_lshl_add_u64 v[10:11], v[10:11], 0, v[14:15]
	s_mov_b32 m0, s4
	v_readfirstlane_b32 s4, v12
	global_load_lds_dwordx4 v[10:11], off
	v_lshl_add_u64 v[10:11], v[10:11], 0, s[6:7]
	s_mov_b32 m0, s4
	s_nop 0
	global_load_lds_dwordx4 v[10:11], off
	s_waitcnt lgkmcnt(0)
	s_barrier
	v_lshlrev_b32_e32 v10, 2, v0
	v_and_b32_e32 v94, 12, v10
	v_or_b32_e32 v120, v94, v61
	v_bitop3_b32 v10, v124, v94, v61 bitop3:0x1e
	v_lshl_or_b32 v14, v10, 4, v18
	v_bitop3_b32 v10, v124, v120, 1 bitop3:0x36
	v_lshl_or_b32 v19, v10, 4, v18
	s_load_dwordx4 s[4:7], s[0:1], 0x20
	s_load_dwordx2 s[12:13], s[0:1], 0x38
	ds_read_b128 v[10:13], v14
	ds_read_b128 v[62:65], v14 offset:8192
	ds_read_b128 v[14:17], v19
	ds_read_b128 v[66:69], v19 offset:8192
	v_bitop3_b32 v19, v124, v120, 4 bitop3:0x36
	v_lshl_or_b32 v19, v19, 4, v18
	v_bitop3_b32 v20, v124, v120, 5 bitop3:0x36
	v_lshl_or_b32 v20, v20, 4, v18
	ds_read_b128 v[70:73], v19
	ds_read_b128 v[78:81], v19 offset:8192
	ds_read_b128 v[74:77], v20
	ds_read_b128 v[82:85], v20 offset:8192
	v_bitop3_b32 v19, v124, v120, 8 bitop3:0x36
	v_lshl_or_b32 v19, v19, 4, v18
	v_bitop3_b32 v20, v124, v120, 9 bitop3:0x36
	v_lshl_or_b32 v20, v20, 4, v18
	ds_read_b128 v[86:89], v19
	ds_read_b128 v[104:107], v19 offset:8192
	ds_read_b128 v[90:93], v20
	ds_read_b128 v[108:111], v20 offset:8192
	v_bitop3_b32 v19, v124, v120, 12 bitop3:0x36
	v_lshl_or_b32 v19, v19, 4, v18
	v_bitop3_b32 v20, v124, v120, 13 bitop3:0x36
	v_lshl_or_b32 v18, v20, 4, v18
	ds_read_b128 v[126:129], v19
	ds_read_b128 v[134:137], v19 offset:8192
	ds_read_b128 v[130:133], v18
	ds_read_b128 v[138:141], v18 offset:8192
	v_mov_b32_e32 v103, 0x7f
	v_lshlrev_b32_e32 v58, 7, v99
	v_or_b32_e32 v122, 0x18000, v117
	s_waitcnt vmcnt(8) lgkmcnt(0)
	v_mfma_scale_f32_32x32x64_f8f6f4 v[18:33], v[2:9], v[10:17], 0, v103, v103 op_sel_hi:[0,0,0]
	v_lshlrev_b32_e32 v125, 3, v119
	v_or_b32_e32 v123, 0x1a000, v117
	v_mfma_scale_f32_32x32x64_f8f6f4 v[2:17], v[2:9], v[62:69], 0, v103, v103 op_sel_hi:[0,0,0]
	v_and_b32_e32 v62, 12, v95
	v_mfma_scale_f32_32x32x64_f8f6f4 v[18:33], v[50:57], v[70:77], v[18:33], v103, v103 op_sel_hi:[0,0,0]
	v_mfma_scale_f32_32x32x64_f8f6f4 v[2:17], v[50:57], v[78:85], v[2:17], v103, v103 op_sel_hi:[0,0,0]
	v_lshl_add_u64 v[50:51], s[10:11], 0, v[58:59]
	v_lshlrev_b32_e32 v58, 4, v119
	v_lshl_add_u64 v[54:55], v[50:51], 0, v[58:59]
	global_load_dwordx4 v[50:53], v[54:55], off
	s_brev_b32 s10, 60
	v_lshlrev_b32_e32 v58, 6, v0
	v_and_b32_e32 v58, 0x4000, v58
	v_or3_b32 v63, v122, v58, v125
	v_or3_b32 v58, v123, v58, v125
	v_mfma_scale_f32_32x32x64_f8f6f4 v[18:33], v[42:49], v[86:93], v[18:33], v103, v103 op_sel_hi:[0,0,0]
	v_mfma_scale_f32_32x32x64_f8f6f4 v[2:17], v[42:49], v[104:111], v[2:17], v103, v103 op_sel_hi:[0,0,0]
	global_load_dwordx4 v[42:45], v[54:55], off offset:32
	global_load_dwordx4 v[46:49], v[54:55], off offset:64
	s_nop 0
	global_load_dwordx4 v[54:57], v[54:55], off offset:96
	v_mfma_scale_f32_32x32x64_f8f6f4 v[2:17], v[34:41], v[134:141], v[2:17], v103, v103 op_sel_hi:[0,0,0]
	v_mfma_scale_f32_32x32x64_f8f6f4 v[18:33], v[34:41], v[126:133], v[18:33], v103, v103 op_sel_hi:[0,0,0]
	s_waitcnt vmcnt(0)
	s_nop 15
	s_nop 1
	v_fma_f32 v2, v2, s10, v50
	v_fma_f32 v3, v3, s10, v51
	v_fma_f32 v4, v4, s10, v52
	v_fma_f32 v5, v5, s10, v53
	v_cvt_pk_f16_f32 v2, v2, v3
	v_cvt_pk_f16_f32 v3, v4, v5
	v_bitop3_b32 v4, v95, v120, 12 bitop3:0x6c
	v_pk_fma_f32 v[18:19], v[18:19], s[10:11], v[50:51] op_sel_hi:[1,0,1]
	v_pk_fma_f32 v[20:21], v[20:21], s[10:11], v[52:53] op_sel_hi:[1,0,1]
	v_lshlrev_b32_e32 v4, 4, v4
	v_cvt_pk_f16_f32 v18, v18, v19
	v_cvt_pk_f16_f32 v19, v20, v21
	v_or_b32_e32 v5, v63, v4
	v_or_b32_e32 v4, v58, v4
	ds_write_b64 v5, v[18:19]
	ds_write_b64 v4, v[2:3]
	v_pk_fma_f32 v[2:3], v[22:23], s[10:11], v[42:43] op_sel_hi:[1,0,1]
	v_pk_fma_f32 v[4:5], v[6:7], s[10:11], v[42:43] op_sel_hi:[1,0,1]
	v_pk_fma_f32 v[6:7], v[24:25], s[10:11], v[44:45] op_sel_hi:[1,0,1]
	v_cvt_pk_f16_f32 v2, v2, v3
	v_cvt_pk_f16_f32 v3, v6, v7
	v_pk_fma_f32 v[6:7], v[8:9], s[10:11], v[44:45] op_sel_hi:[1,0,1]
	v_cvt_pk_f16_f32 v4, v4, v5
	v_cvt_pk_f16_f32 v5, v6, v7
	v_bitop3_b32 v6, v62, v120, 1 bitop3:0x36
	v_lshlrev_b32_e32 v6, 4, v6
	v_or_b32_e32 v7, v63, v6
	ds_write_b64 v7, v[2:3]
	v_or_b32_e32 v2, v58, v6
	ds_write_b64 v2, v[4:5]
	v_pk_fma_f32 v[2:3], v[26:27], s[10:11], v[46:47] op_sel_hi:[1,0,1]
	v_pk_fma_f32 v[6:7], v[28:29], s[10:11], v[48:49] op_sel_hi:[1,0,1]
	v_cvt_pk_f16_f32 v2, v2, v3
	v_pk_fma_f32 v[4:5], v[10:11], s[10:11], v[46:47] op_sel_hi:[1,0,1]
	v_cvt_pk_f16_f32 v3, v6, v7
	v_pk_fma_f32 v[6:7], v[12:13], s[10:11], v[48:49] op_sel_hi:[1,0,1]
	v_cvt_pk_f16_f32 v4, v4, v5
	v_cvt_pk_f16_f32 v5, v6, v7
	v_bitop3_b32 v6, v62, v120, 2 bitop3:0x36
	v_lshlrev_b32_e32 v6, 4, v6
	v_or_b32_e32 v7, v63, v6
	ds_write_b64 v7, v[2:3]
	v_or_b32_e32 v2, v58, v6
	ds_write_b64 v2, v[4:5]
	v_pk_fma_f32 v[2:3], v[30:31], s[10:11], v[54:55] op_sel_hi:[1,0,1]
	v_pk_fma_f32 v[6:7], v[32:33], s[10:11], v[56:57] op_sel_hi:[1,0,1]
	v_cvt_pk_f16_f32 v2, v2, v3
	v_pk_fma_f32 v[4:5], v[14:15], s[10:11], v[54:55] op_sel_hi:[1,0,1]
	v_cvt_pk_f16_f32 v3, v6, v7
	v_pk_fma_f32 v[6:7], v[16:17], s[10:11], v[56:57] op_sel_hi:[1,0,1]
	v_cvt_pk_f16_f32 v4, v4, v5
	v_cvt_pk_f16_f32 v5, v6, v7
	v_bitop3_b32 v6, v62, v120, 3 bitop3:0x36
	v_lshlrev_b32_e32 v6, 4, v6
	v_or_b32_e32 v7, v63, v6
	ds_write_b64 v7, v[2:3]
	v_or_b32_e32 v2, v58, v6
	ds_write_b64 v2, v[4:5]
	s_waitcnt lgkmcnt(0)
	s_barrier
	v_lshrrev_b32_e32 v27, 8, v0
	v_lshrrev_b32_e32 v3, 3, v0
	v_and_b32_e32 v3, 16, v3
	v_mul_u32_u24_e32 v28, 0x60, v27
	v_lshlrev_b32_e32 v26, 5, v27
	v_or_b32_e32 v146, v3, v100
	v_or_b32_e32 v147, v28, v100
	v_or_b32_e32 v4, v146, v26
	v_lshlrev_b32_e32 v209, 2, v4
	v_add_u32_e32 v209, 0x27800, v209
	v_lshlrev_b32_e32 v4, 8, v4
	v_or_b32_e32 v5, 0x18000, v4
	v_bitop3_b32 v11, v101, v120, 12 bitop3:0x36
	v_or_b32_e32 v95, 0x1c000, v4
	v_lshlrev_b32_e32 v29, 3, v101
	v_bitop3_b32 v6, v101, v94, v61 bitop3:0x1e
	v_bitop3_b32 v8, v101, v120, 4 bitop3:0x36
	v_bitop3_b32 v10, v101, v120, 8 bitop3:0x36
	v_lshlrev_b32_e32 v94, 4, v11
	v_lshlrev_b32_e32 v6, 4, v6
	v_lshlrev_b32_e32 v8, 4, v8
	v_lshlrev_b32_e32 v58, 4, v10
	v_or_b32_e32 v7, v5, v6
	v_or_b32_e32 v9, v5, v8
	v_or_b32_e32 v10, v5, v58
	v_or_b32_e32 v5, v5, v94
	v_or_b32_e32 v6, v95, v6
	v_or_b32_e32 v60, v95, v8
	ds_read_b128 v[22:25], v7
	ds_read_b128 v[18:21], v9
	ds_read_b128 v[14:17], v10
	ds_read_b128 v[10:13], v5
	ds_read_b128 v[6:9], v6
	ds_read_b128 v[2:5], v60
	v_bfe_u32 v103, v0, 6, 1
	s_movk_i32 s5, 0x2000
	v_mad_u32_u24 v44, v103, 48, v147
	v_lshlrev_b32_e32 v60, 8, v44
	v_lshlrev_b32_e32 v44, 2, v44
	v_or_b32_e32 v35, v95, v58
	v_lshlrev_b32_e32 v58, 14, v99
	v_and_b32_e32 v44, 12, v44
	v_or_b32_e32 v56, v44, v61
	v_bitop3_b32 v44, v101, v44, v61 bitop3:0x1e
	v_lshl_add_u64 v[32:33], s[8:9], 0, v[58:59]
	v_lshlrev_b32_e32 v58, 4, v98
	v_or_b32_e32 v36, v95, v94
	v_lshl_add_u64 v[88:89], v[32:33], 0, v[58:59]
	v_lshl_or_b32 v57, v44, 4, v60
	ds_read_b128 v[40:43], v35
	ds_read_b128 v[106:109], v36
	s_load_dword s4, s[6:7], 0x0
	global_load_dwordx4 v[36:39], v[88:89], off
	global_load_dwordx4 v[32:35], v[88:89], off offset:1024
	ds_read_b128 v[44:47], v57
	v_bitop3_b32 v48, v101, v56, 4 bitop3:0x36
	v_lshl_or_b32 v62, v48, 4, v60
	ds_read_b128 v[48:51], v62
	v_bitop3_b32 v52, v101, v56, 8 bitop3:0x36
	v_lshl_or_b32 v63, v52, 4, v60
	ds_read_b128 v[52:55], v63
	s_waitcnt lgkmcnt(0)
	v_mfma_f32_16x16x32_f16 v[44:47], v[44:47], v[22:25], 0
	v_bitop3_b32 v64, v101, v56, 12 bitop3:0x36
	ds_read_b128 v[56:59], v57 offset:49152
	v_lshl_or_b32 v60, v64, 4, v60
	v_mfma_f32_16x16x32_f16 v[44:47], v[48:51], v[18:21], v[44:47]
	ds_read_b128 v[68:71], v60
	ds_read_b128 v[72:75], v62 offset:49152
	v_mad_u32_u24 v104, v103, 3, 1
	v_lshlrev_b32_e32 v132, 4, v104
	v_mfma_f32_16x16x32_f16 v[44:47], v[52:55], v[14:17], v[44:47]
	v_add_u32_e32 v52, v132, v147
	global_load_dwordx4 v[64:67], v[88:89], off offset:2048
	global_load_dwordx4 v[48:51], v[88:89], off offset:3072
	ds_read_b128 v[76:79], v63 offset:49152
	ds_read_b128 v[80:83], v60 offset:49152
	s_waitcnt lgkmcnt(3)
	v_mfma_f32_16x16x32_f16 v[44:47], v[68:71], v[10:13], v[44:47]
	v_lshlrev_b32_e32 v60, 8, v52
	v_lshlrev_b32_e32 v52, 2, v52
	v_and_b32_e32 v52, 12, v52
	v_mfma_f32_16x16x32_f16 v[44:47], v[56:59], v[6:9], v[44:47]
	v_or_b32_e32 v62, v52, v61
	v_bitop3_b32 v52, v101, v52, v61 bitop3:0x1e
	v_lshl_or_b32 v63, v52, 4, v60
	s_waitcnt lgkmcnt(2)
	v_mfma_f32_16x16x32_f16 v[44:47], v[72:75], v[2:5], v[44:47]
	ds_read_b128 v[52:55], v63
	v_bitop3_b32 v56, v101, v62, 4 bitop3:0x36
	v_lshl_or_b32 v84, v56, 4, v60
	s_waitcnt lgkmcnt(2)
	v_mfma_f32_16x16x32_f16 v[44:47], v[76:79], v[40:43], v[44:47]
	ds_read_b128 v[56:59], v84
	v_bitop3_b32 v68, v101, v62, 8 bitop3:0x36
	v_lshl_or_b32 v85, v68, 4, v60
	s_waitcnt lgkmcnt(2)
	v_mfma_f32_16x16x32_f16 v[110:113], v[80:83], v[106:109], v[44:47]
	ds_read_b128 v[68:71], v63 offset:49152
	v_bitop3_b32 v62, v101, v62, 12 bitop3:0x36
	v_lshl_or_b32 v60, v62, 4, v60
	ds_read_b128 v[44:47], v85
	s_waitcnt lgkmcnt(3)
	v_mfma_f32_16x16x32_f16 v[52:55], v[52:55], v[22:25], 0
	ds_read_b128 v[72:75], v60
	ds_read_b128 v[76:79], v84 offset:49152
	v_mad_u32_u24 v105, v103, 3, 2
	v_lshlrev_b32_e32 v133, 4, v105
	s_waitcnt lgkmcnt(4)
	v_mfma_f32_16x16x32_f16 v[52:55], v[56:59], v[18:21], v[52:55]
	ds_read_b128 v[56:59], v85 offset:49152
	v_add_co_u32_e32 v114, vcc, s15, v88
	s_waitcnt lgkmcnt(3)
	v_mfma_f32_16x16x32_f16 v[44:47], v[44:47], v[14:17], v[52:55]
	v_addc_co_u32_e32 v115, vcc, 0, v89, vcc
	s_waitcnt lgkmcnt(2)
	v_mfma_f32_16x16x32_f16 v[44:47], v[72:75], v[10:13], v[44:47]
	ds_read_b128 v[52:55], v60 offset:49152
	v_add_u32_e32 v60, v133, v147
	v_lshlrev_b32_e32 v72, 8, v60
	v_lshlrev_b32_e32 v60, 2, v60
	v_mfma_f32_16x16x32_f16 v[44:47], v[68:71], v[6:9], v[44:47]
	v_and_b32_e32 v60, 12, v60
	v_or_b32_e32 v68, v60, v61
	v_bitop3_b32 v60, v101, v60, v61 bitop3:0x1e
	v_lshl_or_b32 v69, v60, 4, v72
	s_waitcnt lgkmcnt(2)
	v_mfma_f32_16x16x32_f16 v[44:47], v[76:79], v[2:5], v[44:47]
	ds_read_b128 v[60:63], v69
	v_bitop3_b32 v70, v101, v68, 4 bitop3:0x36
	v_lshl_or_b32 v70, v70, 4, v72
	s_waitcnt lgkmcnt(2)
	v_mfma_f32_16x16x32_f16 v[44:47], v[56:59], v[40:43], v[44:47]
	ds_read_b128 v[56:59], v70
	v_bitop3_b32 v71, v101, v68, 8 bitop3:0x36
	v_lshl_or_b32 v71, v71, 4, v72
	s_waitcnt lgkmcnt(1)
	v_mfma_f32_16x16x32_f16 v[22:25], v[60:63], v[22:25], 0
	v_bitop3_b32 v60, v101, v68, 12 bitop3:0x36
	v_lshl_or_b32 v68, v60, 4, v72
	ds_read_b32 v210, v209
	v_mfma_f32_16x16x32_f16 v[126:129], v[52:55], v[106:109], v[44:47]
	s_nop 2
	ds_read_b128 v[44:47], v71
	ds_read_b128 v[52:55], v69 offset:49152
	ds_read_b128 v[60:63], v70 offset:49152
	s_waitcnt lgkmcnt(4)
	v_mfma_f32_16x16x32_f16 v[18:21], v[56:59], v[18:21], v[22:25]
	ds_read_b128 v[56:59], v71 offset:49152
	s_nop 1
	ds_read_b128 v[22:25], v68
	s_waitcnt lgkmcnt(4)
	v_mfma_f32_16x16x32_f16 v[14:17], v[44:47], v[14:17], v[18:21]
	v_add_co_u32_e32 v44, vcc, s5, v88
	s_movk_i32 s5, 0x3000
	s_nop 0
	ds_read_b128 v[18:21], v68 offset:49152
	s_waitcnt lgkmcnt(1)
	v_mfma_f32_16x16x32_f16 v[10:13], v[22:25], v[10:13], v[14:17]
	v_addc_co_u32_e32 v45, vcc, 0, v89, vcc
	global_load_dwordx4 v[84:87], v[114:115], off offset:1024
	global_load_dwordx4 v[80:83], v[114:115], off offset:2048
	global_load_dwordx4 v[92:95], v[44:45], off offset:-4096
	global_load_dwordx4 v[76:79], v[44:45], off
	v_mfma_f32_16x16x32_f16 v[6:9], v[52:55], v[6:9], v[10:13]
	global_load_dwordx4 v[72:75], v[44:45], off offset:1024
	global_load_dwordx4 v[68:71], v[44:45], off offset:2048
	global_load_dwordx4 v[52:55], v[44:45], off offset:3072
	v_mov_b32_e32 v13, 0xff61b1e6
	v_mfma_f32_16x16x32_f16 v[2:5], v[60:63], v[2:5], v[6:9]
	s_nop 2
	v_add_co_u32_e32 v6, vcc, s5, v88
	v_mfma_f32_16x16x32_f16 v[2:5], v[56:59], v[40:43], v[2:5]
	s_nop 0
	v_addc_co_u32_e32 v7, vcc, 0, v89, vcc
	global_load_dwordx4 v[88:91], v[114:115], off offset:3072
	global_load_dwordx4 v[60:63], v[6:7], off
	global_load_dwordx4 v[56:59], v[6:7], off offset:1024
	global_load_dwordx4 v[44:47], v[6:7], off offset:2048
	global_load_dwordx4 v[40:43], v[6:7], off offset:3072
	s_waitcnt lgkmcnt(0)
	v_mfma_f32_16x16x32_f16 v[16:19], v[18:21], v[106:109], v[2:5]
	s_mov_b32 s5, 0xff61b1e6
	s_nop 0
	v_or_b32_e32 v3, s14, v146
	v_mov_b32_e32 v4, 0x7df
	v_med3_u32 v3, v3, 32, v4
	v_or_b32_e32 v4, v97, v102
	v_sub_u32_e32 v3, v4, v3
	v_add_f32_e32 v2, s4, v210
	v_add_u32_e32 v3, 32, v3
	v_mad_u32_u24 v4, v103, 48, v3
	s_movk_i32 s4, 0x41
	v_add_f32_e32 v5, v2, v110
	v_mul_f32_e32 v5, 0x3db8aa3b, v5
	v_cmp_gt_u32_e32 vcc, s4, v4
	v_add_u32_e32 v6, 1, v4
	v_add_f32_e32 v7, v2, v111
	v_cndmask_b32_e32 v5, v13, v5, vcc
	v_mul_f32_e32 v7, 0x3db8aa3b, v7
	v_cmp_gt_u32_e32 vcc, s4, v6
	v_add_u32_e32 v8, 2, v4
	v_add_f32_e32 v9, v2, v112
	v_cndmask_b32_e32 v6, v13, v7, vcc
	v_mul_f32_e32 v9, 0x3db8aa3b, v9
	v_cmp_gt_u32_e32 vcc, s4, v8
	v_add_u32_e32 v4, 3, v4
	v_max3_f32 v7, v5, s5, v6
	v_cndmask_b32_e32 v8, v13, v9, vcc
	v_add_f32_e32 v9, v2, v113
	v_mul_f32_e32 v9, 0x3db8aa3b, v9
	v_cmp_gt_u32_e32 vcc, s4, v4
	v_add_u32_e32 v11, v3, v132
	v_add_f32_e32 v12, v2, v127
	v_cndmask_b32_e32 v10, v13, v9, vcc
	v_max3_f32 v4, v7, v8, v10
	v_add_f32_e32 v7, v2, v126
	v_mul_f32_e32 v7, 0x3db8aa3b, v7
	v_cmp_gt_u32_e32 vcc, s4, v11
	v_add_u32_e32 v9, 1, v11
	v_mul_f32_e32 v12, 0x3db8aa3b, v12
	v_cndmask_b32_e32 v7, v13, v7, vcc
	v_cmp_gt_u32_e32 vcc, s4, v9
	v_add_f32_e32 v14, v2, v128
	v_mul_f32_e32 v14, 0x3db8aa3b, v14
	v_cndmask_b32_e32 v9, v13, v12, vcc
	v_add_u32_e32 v12, 2, v11
	v_cmp_gt_u32_e32 vcc, s4, v12
	v_add_u32_e32 v11, 3, v11
	v_add_u32_e32 v3, v3, v133
	v_cndmask_b32_e32 v12, v13, v14, vcc
	v_add_f32_e32 v14, v2, v129
	v_mul_f32_e32 v14, 0x3db8aa3b, v14
	v_cmp_gt_u32_e32 vcc, s4, v11
	v_add_f32_e32 v11, v2, v16
	v_mul_f32_e32 v11, 0x3db8aa3b, v11
	v_cndmask_b32_e32 v15, v13, v14, vcc
	v_cmp_gt_u32_e32 vcc, s4, v3
	v_add_u32_e32 v14, 1, v3
	v_add_f32_e32 v16, v2, v17
	v_cndmask_b32_e32 v11, v13, v11, vcc
	v_mul_f32_e32 v16, 0x3db8aa3b, v16
	v_cmp_gt_u32_e32 vcc, s4, v14
	v_add_f32_e32 v17, v2, v18
	v_max3_f32 v4, v4, v7, v9
	v_cndmask_b32_e32 v14, v13, v16, vcc
	v_add_u32_e32 v16, 2, v3
	v_mul_f32_e32 v17, 0x3db8aa3b, v17
	v_cmp_gt_u32_e32 vcc, s4, v16
	v_add_u32_e32 v3, 3, v3
	v_add_f32_e32 v2, v2, v19
	v_max3_f32 v4, v4, v12, v15
	v_cndmask_b32_e32 v16, v13, v17, vcc
	v_mul_f32_e32 v2, 0x3db8aa3b, v2
	v_cmp_gt_u32_e32 vcc, s4, v3
	v_max3_f32 v4, v4, v11, v14
	v_lshlrev_b32_e32 v126, 5, v99
	v_cndmask_b32_e32 v17, v13, v2, vcc
	v_max3_f32 v2, v4, v16, v17
	v_mov_b32_e32 v3, v2
	v_lshlrev_b32_e32 v127, 2, v119
	v_lshrrev_b32_e32 v4, 7, v0
	v_cmp_gt_u32_e32 vcc, 16, v98
	v_permlane16_swap_b32_e32 v3, v2
	v_max_f32_e32 v2, v2, v3
	v_mov_b32_e32 v3, v2
	s_nop 1
	v_permlane32_swap_b32_e32 v3, v2
	v_max_f32_e32 v13, v2, v3
	v_and_b32_e32 v2, 0x180, v0
	v_or_b32_e32 v2, 0x23400, v2
	v_lshlrev_b32_e32 v3, 2, v100
	s_and_saveexec_b64 s[4:5], vcc
	v_lshlrev_b32_e32 v18, 6, v103
	v_add3_u32 v18, v2, v18, v3
	ds_write_b32 v18, v13
	s_or_b64 exec, exec, s[4:5]
	v_lshlrev_b32_e32 v18, 4, v103
	v_bitop3_b32 v19, v18, 16, v100 bitop3:0x36
	v_lshl_add_u32 v2, v19, 2, v2
	s_waitcnt lgkmcnt(0)
	s_barrier
	ds_read_b32 v19, v2
	v_max_f32_e32 v13, v13, v13
	v_mul_u32_u24_e32 v20, 0xd00, v4
	s_load_dwordx2 s[0:1], s[0:1], 0x30
	v_or_b32_e32 v2, 1, v124
	s_waitcnt lgkmcnt(0)
	v_max_f32_e32 v19, v19, v19
	v_max_f32_e32 v19, v13, v19
	v_sub_f32_e32 v5, v5, v19
	v_exp_f32_e32 v5, v5
	v_sub_f32_e32 v6, v6, v19
	v_exp_f32_e32 v6, v6
	v_sub_f32_e32 v8, v8, v19
	v_mul_u32_u24_e32 v13, 0xd0, v100
	v_exp_f32_e32 v8, v8
	v_sub_f32_e32 v10, v10, v19
	v_add3_u32 v20, v13, v20, v29
	v_exp_f32_e32 v10, v10
	v_or_b32_e32 v22, 0x20000, v20
	v_add_f32_e32 v20, 0, v5
	v_add_f32_e32 v20, v20, v6
	v_add_f32_e32 v20, v20, v8
	v_add_f32_e32 v23, v20, v10
	v_cvt_pk_f16_f32 v21, v8, v10
	v_cvt_pk_f16_f32 v20, v5, v6
	v_mad_u32_u24 v5, v103, s16, v22
	ds_write_b64 v5, v[20:21]
	v_sub_f32_e32 v5, v7, v19
	v_exp_f32_e32 v5, v5
	v_sub_f32_e32 v6, v9, v19
	v_exp_f32_e32 v6, v6
	v_sub_f32_e32 v7, v12, v19
	v_exp_f32_e32 v7, v7
	v_sub_f32_e32 v8, v15, v19
	v_exp_f32_e32 v8, v8
	v_sub_f32_e32 v10, v11, v19
	v_add_f32_e32 v9, v23, v5
	v_exp_f32_e32 v10, v10
	v_sub_f32_e32 v11, v14, v19
	v_add_f32_e32 v9, v9, v6
	v_exp_f32_e32 v11, v11
	v_sub_f32_e32 v12, v16, v19
	v_add_f32_e32 v9, v9, v7
	v_exp_f32_e32 v12, v12
	v_sub_f32_e32 v14, v17, v19
	v_add_f32_e32 v9, v9, v8
	v_exp_f32_e32 v14, v14
	v_add_f32_e32 v9, v9, v10
	v_add_f32_e32 v9, v9, v11
	v_add_f32_e32 v9, v9, v12
	v_add_f32_e32 v9, v9, v14
	v_mov_b32_e32 v15, v9
	v_cvt_pk_f16_f32 v7, v7, v8
	v_cvt_pk_f16_f32 v6, v5, v6
	v_lshl_add_u32 v5, v104, 5, v22
	ds_write_b64 v5, v[6:7]
	v_permlane16_swap_b32_e32 v15, v9
	v_add_f32_e32 v5, v9, v15
	v_mov_b32_e32 v6, v5
	s_movk_i32 s7, 0xd00
	s_mov_b32 s6, 0x20000
	v_cvt_pk_f16_f32 v9, v12, v14
	v_cvt_pk_f16_f32 v8, v10, v11
	v_lshl_add_u32 v7, v105, 5, v22
	ds_write_b64 v7, v[8:9]
	v_permlane32_swap_b32_e32 v6, v5
	s_and_saveexec_b64 s[4:5], vcc
	s_cbranch_execz .LBB1_4
	v_lshlrev_b32_e32 v4, 5, v4
	v_or_b32_e32 v7, v18, v100
	v_lshlrev_b32_e32 v4, 2, v4
	v_lshlrev_b32_e32 v7, 2, v7
	s_mov_b32 s8, 0x23600
	v_add3_u32 v4, v7, v4, s8
	v_add_f32_e32 v5, v5, v6
	ds_write_b32 v4, v5

	.amdhsa_kernel _Z7na_mainPKDF16_PKhS0_PKfS4_S4_S4_Pf
		.amdhsa_group_segment_fixed_size 162048
		.amdhsa_private_segment_fixed_size 0
		.amdhsa_kernarg_size 64
		.amdhsa_user_sgpr_count 2
		.amdhsa_user_sgpr_dispatch_ptr 0
		.amdhsa_user_sgpr_queue_ptr 0
		.amdhsa_user_sgpr_kernarg_segment_ptr 1
		.amdhsa_user_sgpr_dispatch_id 0
		.amdhsa_user_sgpr_kernarg_preload_length 0
		.amdhsa_user_sgpr_kernarg_preload_offset 0
		.amdhsa_user_sgpr_private_segment_size 0
		.amdhsa_uses_dynamic_stack 0
		.amdhsa_enable_private_segment 0
		.amdhsa_system_sgpr_workgroup_id_x 1
		.amdhsa_system_sgpr_workgroup_id_y 0
		.amdhsa_system_sgpr_workgroup_id_z 0
		.amdhsa_system_sgpr_workgroup_info 0
		.amdhsa_system_vgpr_workitem_id 0
		.amdhsa_next_free_vgpr 232
		.amdhsa_next_free_sgpr 96
		.amdhsa_accum_offset 232
		.amdhsa_reserve_vcc 1
		.amdhsa_float_round_mode_32 0
		.amdhsa_float_round_mode_16_64 0
		.amdhsa_float_denorm_mode_32 3
		.amdhsa_float_denorm_mode_16_64 3
		.amdhsa_dx10_clamp 1
		.amdhsa_ieee_mode 1
		.amdhsa_fp16_overflow 0
		.amdhsa_tg_split 0
		.amdhsa_exception_fp_ieee_invalid_op 0
		.amdhsa_exception_fp_denorm_src 0
		.amdhsa_exception_fp_ieee_div_zero 0
		.amdhsa_exception_fp_ieee_overflow 0
		.amdhsa_exception_fp_ieee_underflow 0
		.amdhsa_exception_fp_ieee_inexact 0
		.amdhsa_exception_int_div_zero 0
	.end_amdhsa_kernel

amdhsa.kernels:
  - .agpr_count:     16
    .args:
      - .actual_access:  read_only
        .address_space:  global
        .offset:         0
        .size:           8
        .value_kind:     global_buffer
      - .actual_access:  read_only
        .address_space:  global
        .offset:         8
        .size:           8
        .value_kind:     global_buffer
      - .actual_access:  read_only
        .address_space:  global
        .offset:         16
        .size:           8
        .value_kind:     global_buffer
      - .actual_access:  read_only
        .address_space:  global
        .offset:         24
        .size:           8
        .value_kind:     global_buffer
      - .actual_access:  read_only
        .address_space:  global
        .offset:         32
        .size:           8
        .value_kind:     global_buffer
      - .actual_access:  read_only
        .address_space:  global
        .offset:         40
        .size:           8
        .value_kind:     global_buffer
      - .actual_access:  write_only
        .address_space:  global
        .offset:         48
        .size:           8
        .value_kind:     global_buffer
      - .actual_access:  write_only
        .address_space:  global
        .offset:         56
        .size:           8
        .value_kind:     global_buffer
      - .actual_access:  write_only
        .address_space:  global
        .offset:         64
        .size:           8
        .value_kind:     global_buffer
      - .actual_access:  write_only
        .address_space:  global
        .offset:         72
        .size:           8
        .value_kind:     global_buffer
      - .actual_access:  write_only
        .address_space:  global
        .offset:         80
        .size:           8
        .value_kind:     global_buffer
      - .actual_access:  write_only
        .address_space:  global
        .offset:         88
        .size:           8
        .value_kind:     global_buffer
    .group_segment_fixed_size: 16384
    .kernarg_segment_align: 8
    .kernarg_segment_size: 96
    .language:       OpenCL C
    .language_version:
      - 2
      - 0
    .max_flat_workgroup_size: 256
    .name:           _Z7na_prepPKfS0_S0_S0_S0_S0_PDF16_PhS1_PfS3_S3_
    .private_segment_fixed_size: 0
    .sgpr_count:     23
    .sgpr_spill_count: 0
    .symbol:         _Z7na_prepPKfS0_S0_S0_S0_S0_PDF16_PhS1_PfS3_S3_.kd
    .uniform_work_group_size: 1
    .uses_dynamic_stack: false
    .vgpr_count:     116
    .vgpr_spill_count: 0
    .wavefront_size: 64
  - .agpr_count:     0
    .args:
      - .address_space:  global
        .offset:         0
        .size:           8
        .value_kind:     global_buffer
      - .actual_access:  read_only
        .address_space:  global
        .offset:         8
        .size:           8
        .value_kind:     global_buffer
      - .actual_access:  read_only
        .address_space:  global
        .offset:         16
        .size:           8
        .value_kind:     global_buffer
      - .actual_access:  read_only
        .address_space:  global
        .offset:         24
        .size:           8
        .value_kind:     global_buffer
      - .actual_access:  read_only
        .address_space:  global
        .offset:         32
        .size:           8
        .value_kind:     global_buffer
      - .actual_access:  read_only
        .address_space:  global
        .offset:         40
        .size:           8
        .value_kind:     global_buffer
      - .actual_access:  read_only
        .address_space:  global
        .offset:         48
        .size:           8
        .value_kind:     global_buffer
      - .actual_access:  write_only
        .address_space:  global
        .offset:         56
        .size:           8
        .value_kind:     global_buffer
    .group_segment_fixed_size: 162048
    .kernarg_segment_align: 8
    .kernarg_segment_size: 64
    .language:       OpenCL C
    .language_version:
      - 2
      - 0
    .max_flat_workgroup_size: 512
    .name:           _Z7na_mainPKDF16_PKhS0_PKfS4_S4_S4_Pf
    .private_segment_fixed_size: 0
    .sgpr_count:     24
    .sgpr_spill_count: 0
    .symbol:         _Z7na_mainPKDF16_PKhS0_PKfS4_S4_S4_Pf.kd
    .uniform_work_group_size: 1
    .uses_dynamic_stack: false
    .vgpr_count:     232
    .vgpr_spill_count: 0
    .wavefront_size: 64
